# v65 + NA deferred row-sum exchange (all work-removing edits combined)
# speedup vs baseline: 1.0011x; 1.0011x over previous
.LBB0_814:
	s_add_i32 s24, s23, -3
	ds_read_b128 v[64:67], v198 offset:49152
	ds_read_b128 v[68:71], v198 offset:57344
	ds_read_b128 v[212:215], v200 offset:49152
	ds_read_b128 v[216:219], v200 offset:57344
	v_exp_f32_e32 v160, v160
	v_exp_f32_e32 v161, v161
	s_waitcnt lgkmcnt(3)
	v_mfma_f32_32x32x16_bf16 v[80:95], v[64:67], v[120:123], 0
	v_exp_f32_e32 v152, v152
	v_exp_f32_e32 v153, v153
	v_exp_f32_e32 v158, v158
	v_exp_f32_e32 v150, v150
	v_exp_f32_e32 v159, v159
	v_exp_f32_e32 v151, v151
	v_exp_f32_e32 v156, v156
	s_waitcnt lgkmcnt(2)
	v_mfma_f32_32x32x16_bf16 v[64:79], v[68:71], v[120:123], 0
	v_exp_f32_e32 v148, v148
	v_exp_f32_e32 v157, v157
	v_exp_f32_e32 v149, v149
	v_add_f32_e32 v162, v176, v211
	v_add_f32_e32 v180, v166, v173
	v_add_f32_e32 v194, v160, v161
	v_add_f32_e32 v195, v152, v153
	s_waitcnt lgkmcnt(1)
	v_mfma_f32_32x32x16_bf16 v[80:95], v[212:215], v[124:127], v[80:95]
	v_exp_f32_e32 v154, v154
	v_exp_f32_e32 v146, v146
	v_add_f32_e32 v162, v163, v162
	v_add_f32_e32 v180, v167, v180
	v_add_f32_e32 v194, v158, v194
	v_add_f32_e32 v195, v150, v195
	v_exp_f32_e32 v155, v155
	s_waitcnt lgkmcnt(0)
	v_mfma_f32_32x32x16_bf16 v[64:79], v[216:219], v[124:127], v[64:79]
	ds_read_b128 v[212:215], v199 offset:49152
	ds_read_b128 v[216:219], v199 offset:57344
	v_exp_f32_e32 v147, v147
	v_add_f32_e32 v162, v177, v162
	v_add_f32_e32 v180, v172, v180
	v_add_f32_e32 v194, v159, v194
	v_add_f32_e32 v195, v151, v195
	v_add_f32_e32 v162, v164, v162
	s_waitcnt lgkmcnt(1)
	v_mfma_f32_32x32x16_bf16 v[80:95], v[212:215], v[116:119], v[80:95]
	v_add_f32_e32 v180, v168, v180
	v_add_f32_e32 v194, v156, v194
	v_add_f32_e32 v195, v148, v195
	v_add_f32_e32 v162, v175, v162
	v_add_f32_e32 v180, v171, v180
	v_add_f32_e32 v194, v157, v194
	v_add_f32_e32 v195, v149, v195
	s_waitcnt lgkmcnt(0)
	v_mfma_f32_32x32x16_bf16 v[64:79], v[216:219], v[116:119], v[64:79]
	ds_read_b128 v[212:215], v193 offset:49152
	ds_read_b128 v[216:219], v193 offset:57344
	v_add_f32_e32 v162, v165, v162
	v_add_f32_e32 v180, v169, v180
	v_add_f32_e32 v194, v154, v194
	v_add_f32_e32 v195, v146, v195
	v_add_f32_e32 v162, v174, v162
	s_waitcnt lgkmcnt(1)
	v_mfma_f32_32x32x16_bf16 v[80:95], v[212:215], v[112:115], v[80:95]
	v_add_f32_e32 v180, v170, v180
	v_add_f32_e32 v194, v155, v194
	v_add_f32_e32 v195, v147, v195
	v_add_f32_e32 v162, v180, v162
	v_add_f32_e32 v180, v195, v194
	v_add_f32_e32 v209, v162, v180
	s_waitcnt lgkmcnt(0)
	v_mfma_f32_32x32x16_bf16 v[64:79], v[216:219], v[112:115], v[64:79]
	ds_read_b128 v[212:215], v192 offset:49152
	ds_read_b128 v[216:219], v192 offset:57344
	s_waitcnt lgkmcnt(0)
	v_mfma_f32_32x32x16_bf16 v[80:95], v[212:215], v[108:111], v[80:95]
	v_mfma_f32_32x32x16_bf16 v[64:79], v[216:219], v[108:111], v[64:79]
	ds_read_b128 v[212:215], v191 offset:49152
	ds_read_b128 v[216:219], v191 offset:57344
	s_waitcnt lgkmcnt(0)
	v_mfma_f32_32x32x16_bf16 v[80:95], v[212:215], v[104:107], v[80:95]
	v_mfma_f32_32x32x16_bf16 v[64:79], v[216:219], v[104:107], v[64:79]
	ds_read_b128 v[212:215], v190 offset:49152
	ds_read_b128 v[216:219], v190 offset:57344
	s_waitcnt lgkmcnt(0)
	v_mfma_f32_32x32x16_bf16 v[80:95], v[212:215], v[100:103], v[80:95]
	v_mfma_f32_32x32x16_bf16 v[64:79], v[216:219], v[100:103], v[64:79]
	ds_read_b128 v[212:215], v189 offset:49152
	ds_read_b128 v[216:219], v189 offset:57344
	v_cvt_pk_bf16_f32 v162, v176, v211
	v_cvt_pk_bf16_f32 v163, v163, v177
	v_cvt_pk_bf16_f32 v164, v164, v175
	v_cvt_pk_bf16_f32 v165, v165, v174
	v_cvt_pk_bf16_f32 v166, v166, v173
	v_cvt_pk_bf16_f32 v167, v167, v172
	s_waitcnt lgkmcnt(1)
	v_mfma_f32_32x32x16_bf16 v[80:95], v[212:215], v[96:99], v[80:95]
	v_cvt_pk_bf16_f32 v168, v168, v171
	v_cvt_pk_bf16_f32 v169, v169, v170
	v_cvt_pk_bf16_f32 v170, v160, v161
	v_cvt_pk_bf16_f32 v171, v158, v159
	v_cvt_pk_bf16_f32 v172, v156, v157
	v_cvt_pk_bf16_f32 v173, v154, v155
	v_cvt_pk_bf16_f32 v174, v152, v153
	s_waitcnt lgkmcnt(0)
	v_mfma_f32_32x32x16_bf16 v[64:79], v[216:219], v[96:99], v[64:79]
	v_cvt_pk_bf16_f32 v175, v150, v151
	v_cvt_pk_bf16_f32 v176, v148, v149
	v_cvt_pk_bf16_f32 v177, v146, v147
	s_cmp_gt_u32 s24, 1
	s_mov_b64 s[10:11], -1
	s_cbranch_scc0 .LBB0_816
	s_add_i32 s25, s17, s23
	s_add_i32 s2, s25, -5
	s_min_i32 s2, s2, s18
	s_lshl_b32 s2, s2, 6
	s_addk_i32 s2, 0x100
	s_mov_b64 s[10:11], 0

.LBB0_825:
	v_cndmask_b32_e64 v206, v65, v206, s[58:59]
	v_mul_f32_e32 v138, 0xbe0293ee, v206
	v_fmamk_f32 v65, v162, 0x3e0293ee, v138
	v_fmamk_f32 v66, v163, 0x3e0293ee, v138
	v_fmamk_f32 v67, v164, 0x3e0293ee, v138
	v_fmamk_f32 v68, v165, 0x3e0293ee, v138
	v_fmamk_f32 v69, v166, 0x3e0293ee, v138
	v_fmamk_f32 v70, v167, 0x3e0293ee, v138
	v_fmamk_f32 v73, v168, 0x3e0293ee, v138
	v_fmamk_f32 v74, v169, 0x3e0293ee, v138
	v_fmamk_f32 v75, v170, 0x3e0293ee, v138
	v_fmamk_f32 v76, v171, 0x3e0293ee, v138
	v_fmamk_f32 v77, v172, 0x3e0293ee, v138
	v_fmamk_f32 v78, v173, 0x3e0293ee, v138
	v_fmamk_f32 v80, v174, 0x3e0293ee, v138
	v_fmamk_f32 v81, v175, 0x3e0293ee, v138
	v_fmamk_f32 v82, v176, 0x3e0293ee, v138
	v_fmamk_f32 v83, v177, 0x3e0293ee, v138
	v_exp_f32_e32 v170, v65
	v_exp_f32_e32 v171, v66
	v_exp_f32_e32 v172, v67
	v_exp_f32_e32 v173, v68
	v_exp_f32_e32 v174, v69
	v_exp_f32_e32 v175, v70
	v_exp_f32_e32 v176, v73
	v_exp_f32_e32 v177, v74
	v_fmamk_f32 v162, v71, 0x3e0293ee, v138
	v_fmamk_f32 v163, v72, 0x3e0293ee, v138
	v_fmamk_f32 v164, v217, 0x3e0293ee, v138
	v_fmamk_f32 v165, v218, 0x3e0293ee, v138
	v_fmamk_f32 v166, v219, 0x3e0293ee, v138
	v_fmamk_f32 v167, v220, 0x3e0293ee, v138
	v_fmamk_f32 v168, v221, 0x3e0293ee, v138
	v_fmamk_f32 v169, v222, 0x3e0293ee, v138
	v_fmamk_f32 v139, v64, 0x3e0293ee, v138
	v_fmamk_f32 v140, v211, 0x3e0293ee, v138
	v_fmamk_f32 v141, v212, 0x3e0293ee, v138
	v_fmamk_f32 v142, v213, 0x3e0293ee, v138
	v_fmamk_f32 v143, v214, 0x3e0293ee, v138
	v_fmamk_f32 v144, v215, 0x3e0293ee, v138
	v_fmamk_f32 v145, v216, 0x3e0293ee, v138
	v_fmac_f32_e32 v138, 0x3e0293ee, v79
	v_exp_f32_e32 v194, v75
	v_exp_f32_e32 v195, v76
	v_exp_f32_e32 v196, v77
	v_exp_f32_e32 v197, v78
	v_exp_f32_e32 v211, v80
	v_exp_f32_e32 v214, v81
	v_exp_f32_e32 v215, v82
	v_exp_f32_e32 v216, v83
	s_waitcnt lgkmcnt(0)
	s_barrier
	ds_read_b128 v[64:67], v198 offset:32768
	ds_read_b128 v[68:71], v198 offset:40960
	ds_read_b128 v[130:133], v200 offset:32768
	ds_read_b128 v[134:137], v200 offset:40960
	v_exp_f32_e32 v138, v138
	s_waitcnt lgkmcnt(2)
	v_mfma_f32_32x32x16_bf16 v[80:95], v[64:67], v[120:123], 0
	v_mfma_f32_32x32x16_bf16 v[64:79], v[68:71], v[120:123], 0
	s_waitcnt lgkmcnt(0)
	v_mfma_f32_32x32x16_bf16 v[80:95], v[130:133], v[124:127], v[80:95]
	v_mfma_f32_32x32x16_bf16 v[64:79], v[134:137], v[124:127], v[64:79]
	ds_read_b128 v[130:133], v199 offset:32768
	ds_read_b128 v[134:137], v199 offset:40960
	s_waitcnt lgkmcnt(0)
	v_mfma_f32_32x32x16_bf16 v[80:95], v[130:133], v[116:119], v[80:95]
	v_mfma_f32_32x32x16_bf16 v[64:79], v[134:137], v[116:119], v[64:79]
	ds_read_b128 v[130:133], v193 offset:32768
	ds_read_b128 v[134:137], v193 offset:40960
	s_waitcnt lgkmcnt(0)
	v_mfma_f32_32x32x16_bf16 v[80:95], v[130:133], v[112:115], v[80:95]
	v_mfma_f32_32x32x16_bf16 v[64:79], v[134:137], v[112:115], v[64:79]
	ds_read_b128 v[130:133], v192 offset:32768
	ds_read_b128 v[134:137], v192 offset:40960
	s_waitcnt lgkmcnt(0)
	v_mfma_f32_32x32x16_bf16 v[80:95], v[130:133], v[108:111], v[80:95]
	v_mfma_f32_32x32x16_bf16 v[64:79], v[134:137], v[108:111], v[64:79]
	ds_read_b128 v[130:133], v191 offset:32768
	ds_read_b128 v[134:137], v191 offset:40960
	s_waitcnt lgkmcnt(0)
	v_mfma_f32_32x32x16_bf16 v[80:95], v[130:133], v[104:107], v[80:95]
	v_mfma_f32_32x32x16_bf16 v[64:79], v[134:137], v[104:107], v[64:79]
	ds_read_b128 v[130:133], v190 offset:32768
	ds_read_b128 v[134:137], v190 offset:40960
	s_waitcnt lgkmcnt(0)
	v_mfma_f32_32x32x16_bf16 v[80:95], v[130:133], v[100:103], v[80:95]
	v_mfma_f32_32x32x16_bf16 v[64:79], v[134:137], v[100:103], v[64:79]
	ds_read_b128 v[130:133], v189 offset:32768
	ds_read_b128 v[134:137], v189 offset:40960
	s_waitcnt lgkmcnt(1)
	v_mfma_f32_32x32x16_bf16 v[80:95], v[130:133], v[96:99], v[80:95]
	v_exp_f32_e32 v130, v139
	v_exp_f32_e32 v131, v140
	v_exp_f32_e32 v139, v163
	v_exp_f32_e32 v140, v164
	v_exp_f32_e32 v132, v141
	v_exp_f32_e32 v141, v165
	v_exp_f32_e32 v133, v142
	v_exp_f32_e32 v142, v166
	s_waitcnt lgkmcnt(0)
	v_mfma_f32_32x32x16_bf16 v[64:79], v[134:137], v[96:99], v[64:79]
	v_exp_f32_e32 v134, v143
	v_exp_f32_e32 v143, v167
	v_exp_f32_e32 v135, v144
	v_exp_f32_e32 v137, v162
	v_exp_f32_e32 v144, v168
	v_add_f32_e32 v162, v170, v171
	v_add_f32_e32 v163, v194, v195
	v_add_f32_e32 v164, v130, v131
	v_add_f32_e32 v165, v139, v140
	v_exp_f32_e32 v136, v145
	v_exp_f32_e32 v145, v169
	v_add_f32_e32 v162, v172, v162
	v_add_f32_e32 v163, v196, v163
	v_add_f32_e32 v164, v132, v164
	v_add_f32_e32 v165, v141, v165
	v_add_f32_e32 v162, v173, v162
	v_add_f32_e32 v163, v197, v163
	v_add_f32_e32 v164, v133, v164
	v_add_f32_e32 v165, v142, v165
	v_add_f32_e32 v162, v174, v162
	v_add_f32_e32 v163, v211, v163
	v_add_f32_e32 v164, v134, v164
	v_add_f32_e32 v165, v143, v165
	v_add_f32_e32 v162, v175, v162
	v_add_f32_e32 v163, v214, v163
	v_add_f32_e32 v164, v135, v164
	v_add_f32_e32 v165, v144, v165
	v_add_f32_e32 v162, v176, v162
	v_add_f32_e32 v163, v215, v163
	v_add_f32_e32 v164, v136, v164
	v_add_f32_e32 v165, v145, v165
	v_add_f32_e32 v162, v177, v162
	v_add_f32_e32 v163, v216, v163
	v_add_f32_e32 v164, v137, v164
	v_add_f32_e32 v165, v138, v165
	v_add_f32_e32 v162, v163, v162
	v_add_f32_e32 v163, v165, v164
	v_add_f32_e32 v212, v163, v162
	v_cvt_pk_bf16_f32 v162, v170, v171
	v_cvt_pk_bf16_f32 v163, v172, v173
	v_cvt_pk_bf16_f32 v164, v174, v175
	v_cvt_pk_bf16_f32 v165, v176, v177
	v_cvt_pk_bf16_f32 v166, v194, v195
	v_cvt_pk_bf16_f32 v167, v196, v197
	v_cvt_pk_bf16_f32 v168, v211, v214
	v_cvt_pk_bf16_f32 v169, v215, v216
	v_cvt_pk_bf16_f32 v170, v130, v131
	v_cvt_pk_bf16_f32 v171, v132, v133
	v_cvt_pk_bf16_f32 v172, v134, v135
	v_cvt_pk_bf16_f32 v173, v136, v137
	v_cvt_pk_bf16_f32 v174, v139, v140
	v_cvt_pk_bf16_f32 v175, v141, v142
	v_cvt_pk_bf16_f32 v176, v143, v144
	v_cvt_pk_bf16_f32 v177, v145, v138
	s_min_i32 s3, s23, s21
	s_cmp_gt_i32 s3, 3
	s_mov_b64 s[10:11], -1
	s_cbranch_scc0 .LBB0_827
	s_add_i32 s2, s3, s20
	s_min_i32 s2, s2, s18
	s_lshl_b32 s2, s2, 6
	s_addk_i32 s2, 0x100
	s_mov_b64 s[10:11], 0
